# idx unit Q staging loads batched; next-layer branch/out weight conversion moved to the low CUs of the gate phase
# speedup vs baseline: 1.0124x; 1.0009x over previous
.LBB0_506:
	s_or_b64 exec, exec, s[8:9]
	v_mov_b32_e32 v1, s12
	s_waitcnt lgkmcnt(0)
	s_barrier
	ds_read_b32 v1, v1
	s_movk_i32 s8, 0x1ff
	s_waitcnt lgkmcnt(0)
	v_cmp_lt_i32_e32 vcc, s8, v1
	v_readfirstlane_b32 s16, v1
	s_mov_b64 s[8:9], -1
	s_cbranch_vccnz .LBB0_503
	v_mov_b32_e32 v1, v0
	s_lshl_b32 s15, s16, 3
	v_readlane_b32 s8, v252, 0
	v_readfirstlane_b32 s17, v1
	s_mov_b32 s9, s88
	s_andn2_b32 s15, s15, 31
	s_ashr_i32 s14, s17, 6
	s_mov_b64 s[10:11], s[68:69]
	s_add_u32 s8, s10, 0x9000000
	s_addc_u32 s9, s11, 0
	s_lshl_b32 s16, s16, 12
	s_and_b32 s18, s16, 0x3000
	s_sub_i32 s16, s18, s15
	s_addk_i32 s16, 0xfe0
	s_waitcnt vmcnt(0)
	v_ashrrev_i32_e32 v9, 7, v1
	v_lshlrev_b32_e32 v2, 4, v1
	v_add_u32_e32 v4, s16, v9
	v_mov_b64_e32 v[10:11], s[10:11]
	s_movk_i32 s19, 0xc00
	v_and_b32_e32 v2, 0x7f0, v2
	v_mad_i64_i32 v[4:5], s[20:21], v4, s19, v[10:11]
	v_lshl_add_u64 v[4:5], v[4:5], 0, v[2:3]
	s_mov_b32 s22, 0x2de00000
	v_add_co_u32_e32 v4, vcc, s22, v4
	s_nop 1
	v_addc_co_u32_e32 v5, vcc, 0, v5, vcc
	v_add_u32_e32 v8, s72, v2
	s_movk_i32 s23, 0x810
	global_load_dwordx4 v[146:149], v[4:5], off offset:1024
	v_mad_u64_u32 v[178:179], s[20:21], v9, s23, v[8:9]
	s_sub_i32 s15, 0x1020, s15
	s_lshr_b32 s15, s15, 6
	v_add_u32_e32 v4, 0x200, v1
	v_ashrrev_i32_e32 v9, 7, v4
	v_add_u32_e32 v4, s16, v9
	v_mad_i64_i32 v[4:5], s[20:21], v4, s19, v[10:11]
	v_lshl_add_u64 v[4:5], v[4:5], 0, v[2:3]
	v_add_co_u32_e32 v4, vcc, s22, v4
	v_mad_u64_u32 v[180:181], s[20:21], v9, s23, v[8:9]
	s_nop 0
	v_addc_co_u32_e32 v5, vcc, 0, v5, vcc
	global_load_dwordx4 v[150:153], v[4:5], off offset:1024
	v_add_u32_e32 v4, 0x400, v1
	v_ashrrev_i32_e32 v9, 7, v4
	v_add_u32_e32 v4, s16, v9
	v_mad_i64_i32 v[4:5], s[20:21], v4, s19, v[10:11]
	v_lshl_add_u64 v[4:5], v[4:5], 0, v[2:3]
	v_add_co_u32_e32 v4, vcc, s22, v4
	v_mad_u64_u32 v[182:183], s[20:21], v9, s23, v[8:9]
	s_nop 0
	v_addc_co_u32_e32 v5, vcc, 0, v5, vcc
	global_load_dwordx4 v[154:157], v[4:5], off offset:1024
	v_add_u32_e32 v4, 0x600, v1
	v_ashrrev_i32_e32 v9, 7, v4
	v_add_u32_e32 v4, s16, v9
	v_mad_i64_i32 v[4:5], s[20:21], v4, s19, v[10:11]
	v_lshl_add_u64 v[4:5], v[4:5], 0, v[2:3]
	v_add_co_u32_e32 v4, vcc, s22, v4
	v_mad_u64_u32 v[184:185], s[20:21], v9, s23, v[8:9]
	s_nop 0
	v_addc_co_u32_e32 v5, vcc, 0, v5, vcc
	global_load_dwordx4 v[158:161], v[4:5], off offset:1024
	v_add_u32_e32 v4, 0x800, v1
	v_ashrrev_i32_e32 v9, 7, v4
	v_add_u32_e32 v4, s16, v9
	v_mad_i64_i32 v[4:5], s[20:21], v4, s19, v[10:11]
	v_lshl_add_u64 v[4:5], v[4:5], 0, v[2:3]
	v_add_co_u32_e32 v4, vcc, s22, v4
	v_mad_u64_u32 v[186:187], s[20:21], v9, s23, v[8:9]
	s_nop 0
	v_addc_co_u32_e32 v5, vcc, 0, v5, vcc
	global_load_dwordx4 v[162:165], v[4:5], off offset:1024
	v_add_u32_e32 v4, 0xa00, v1
	v_ashrrev_i32_e32 v9, 7, v4
	v_add_u32_e32 v4, s16, v9
	v_mad_i64_i32 v[4:5], s[20:21], v4, s19, v[10:11]
	v_lshl_add_u64 v[4:5], v[4:5], 0, v[2:3]
	v_add_co_u32_e32 v4, vcc, s22, v4
	v_mad_u64_u32 v[188:189], s[20:21], v9, s23, v[8:9]
	s_nop 0
	v_addc_co_u32_e32 v5, vcc, 0, v5, vcc
	global_load_dwordx4 v[166:169], v[4:5], off offset:1024
	v_add_u32_e32 v4, 0xc00, v1
	v_ashrrev_i32_e32 v9, 7, v4
	v_add_u32_e32 v4, s16, v9
	v_mad_i64_i32 v[4:5], s[20:21], v4, s19, v[10:11]
	v_lshl_add_u64 v[4:5], v[4:5], 0, v[2:3]
	v_add_co_u32_e32 v4, vcc, s22, v4
	v_mad_u64_u32 v[190:191], s[20:21], v9, s23, v[8:9]
	s_nop 0
	v_addc_co_u32_e32 v5, vcc, 0, v5, vcc
	global_load_dwordx4 v[170:173], v[4:5], off offset:1024
	v_add_u32_e32 v4, 0xe00, v1
	v_ashrrev_i32_e32 v9, 7, v4
	v_add_u32_e32 v4, s16, v9
	v_mad_i64_i32 v[4:5], s[20:21], v4, s19, v[10:11]
	v_lshl_add_u64 v[4:5], v[4:5], 0, v[2:3]
	v_add_co_u32_e32 v4, vcc, s22, v4
	v_mad_u64_u32 v[192:193], s[20:21], v9, s23, v[8:9]
	s_nop 0
	v_addc_co_u32_e32 v5, vcc, 0, v5, vcc
	global_load_dwordx4 v[174:177], v[4:5], off offset:1024
	s_movk_i32 s19, 0x3000
	v_ashrrev_i32_e32 v6, 4, v1
	v_and_b32_e32 v7, 15, v1
	v_add_u32_e32 v2, s16, v6
	v_mov_b64_e32 v[4:5], s[8:9]
	v_mad_i64_i32 v[4:5], s[20:21], v2, s24, v[4:5]
	v_lshlrev_b32_e32 v2, 1, v7
	v_lshl_add_u64 v[4:5], v[4:5], 0, v[2:3]
	v_add_co_u32_e32 v4, vcc, s19, v4
	s_mov_b64 s[20:21], 0x3100
	s_nop 0
	v_addc_co_u32_e32 v5, vcc, 0, v5, vcc
	global_load_ushort v2, v[4:5], off offset:384
	v_lshlrev_b32_e32 v4, 7, v7
	v_lshlrev_b32_e32 v5, 2, v6
	v_add3_u32 v4, s13, v4, v5
	s_cmp_ge_i32 s14, s15
	s_barrier
	s_waitcnt vmcnt(8)
	ds_write_b128 v178, v[146:149]
	s_waitcnt vmcnt(7)
	ds_write_b128 v180, v[150:153]
	s_waitcnt vmcnt(6)
	ds_write_b128 v182, v[154:157]
	s_waitcnt vmcnt(5)
	ds_write_b128 v184, v[158:161]
	s_waitcnt vmcnt(4)
	ds_write_b128 v186, v[162:165]
	s_waitcnt vmcnt(3)
	ds_write_b128 v188, v[166:169]
	s_waitcnt vmcnt(2)
	ds_write_b128 v190, v[170:173]
	s_waitcnt vmcnt(1)
	ds_write_b128 v192, v[174:177]
	s_waitcnt vmcnt(0)
	v_lshlrev_b32_e32 v2, 16, v2
	v_mul_f32_e32 v2, 0x3d000000, v2
	ds_write_b32 v4, v2
	s_waitcnt lgkmcnt(0)
	s_barrier
	s_cbranch_scc1 .LBB0_502
	s_andn2_b32 s17, s17, 63
	v_and_b32_e32 v5, 31, v1
	s_add_i32 s17, s17, s18
	v_or_b32_e32 v12, s17, v5
	v_bfe_u32 v2, v1, 5, 1
	v_or_b32_e32 v8, 32, v12
	v_mov_b64_e32 v[6:7], s[8:9]
	v_lshlrev_b32_e32 v4, 3, v2
	v_or_b32_e32 v1, s18, v5
	v_mad_i64_i32 v[8:9], s[18:19], v8, s24, v[6:7]
	v_lshlrev_b32_e32 v2, 4, v2
	v_lshl_add_u64 v[8:9], v[8:9], 0, v[2:3]
	s_movk_i32 s17, 0x3000
	v_lshl_add_u64 v[10:11], v[8:9], 0, s[20:21]
	v_add_co_u32_e32 v8, vcc, s17, v8
	v_mad_i64_i32 v[6:7], s[18:19], v12, s24, v[6:7]
	s_nop 0
	v_addc_co_u32_e32 v9, vcc, 0, v9, vcc
	v_lshl_add_u64 v[6:7], v[6:7], 0, v[2:3]
	global_load_dwordx4 v[36:39], v[10:11], off offset:96
	global_load_dwordx4 v[44:47], v[10:11], off offset:64
	global_load_dwordx4 v[40:43], v[10:11], off offset:32
	global_load_dwordx4 v[48:51], v[8:9], off offset:256
	v_lshl_add_u64 v[8:9], v[6:7], 0, s[20:21]
	v_add_co_u32_e32 v6, vcc, s17, v6
	global_load_dwordx4 v[52:55], v[8:9], off offset:96
	global_load_dwordx4 v[60:63], v[8:9], off offset:64
	global_load_dwordx4 v[56:59], v[8:9], off offset:32
	v_addc_co_u32_e32 v7, vcc, 0, v7, vcc
	global_load_dwordx4 v[64:67], v[6:7], off offset:256
	v_mul_u32_u24_e32 v6, 0x810, v5
	v_lshl_add_u32 v134, v5, 2, s13
	v_add3_u32 v135, s72, v6, v2
	v_or_b32_e32 v5, s16, v5
	v_mov_b64_e32 v[6:7], s[10:11]
	s_movk_i32 s10, 0x4100
	v_mad_u64_u32 v[6:7], s[10:11], v5, s10, v[6:7]
	v_lshl_add_u64 v[6:7], v[6:7], 0, v[2:3]
	s_mov_b64 s[10:11], 0x30e00000
	v_lshl_add_u64 v[132:133], v[6:7], 0, s[10:11]
	v_lshlrev_b32_e32 v2, 1, v4
	s_waitcnt vmcnt(0)

.LBB0_1845:
	s_mov_b32 s100, s4
	s_cmp_lg_u32 s28, 0x100
	s_cbranch_scc1 .Lcvl_std
	s_xor_b32 s100, s4, 0x80
.Lcvl_std:
	v_readlane_b32 s0, v253, 24
	v_readlane_b32 s1, v253, 25
	s_cmp_lg_u32 s0, 3
	s_cselect_b64 s[0:1], -1, 0
	s_cmpk_gt_i32 s100, 0x7f
	s_cselect_b64 s[6:7], -1, 0
	s_and_b64 s[0:1], s[0:1], s[6:7]
	s_andn2_b64 vcc, exec, s[0:1]
	s_cbranch_vccnz .LBB0_1854
	s_lshl_b32 s0, s100, 3
	s_add_i32 s0, s30, s0
	s_add_i32 s10, s0, 0xfffffc00
	s_cmpk_gt_i32 s10, 0x7ff
	s_cbranch_scc1 .LBB0_1854
	v_readlane_b32 s0, v253, 24
	s_lshl_b32 s11, s28, 3
	s_lshl_b32 s0, s0, 24
	s_addk_i32 s11, 0xfc00
	s_add_i32 s0, s0, 0x1000000
	v_readlane_b32 s4, v253, 17
	s_add_i32 s12, s72, 0x210a0
	v_readlane_b32 s1, v253, 25
	v_readlane_b32 s5, v253, 18
	s_add_u32 s4, s2, 0x4500000
	s_mov_b32 s1, s5
	s_addc_u32 s5, s3, 0
	s_add_i32 s13, s72, 0x21098
	s_add_u32 s14, s2, 0x3d00000
	s_addc_u32 s15, s3, 0
	s_lshl_b32 s2, s10, 1
	v_and_b32_e32 v1, 63, v1
	s_add_i32 s16, s2, 0x1f800
	s_lshl_b32 s17, s11, 1
	s_lshl_b32 s18, s10, 6
	s_lshl_b32 s19, s11, 6
	v_readlane_b32 s6, v253, 19
	v_readlane_b32 s7, v253, 20
	s_branch .LBB0_1850
